# scan-A work queue: next-item ticket atomic no longer waited for at issue; waited at the next loop top (on top of v33)
# speedup vs baseline: 1.0028x; 1.0028x over previous
.LBB0_551:
	s_barrier
	v_mov_b32 v2, v0
	s_nop 0
	v_cmp_eq_u32_e32 vcc, 0, v2
	s_and_saveexec_b64 s[0:1], vcc
	s_cbranch_execz .Ltkt_a_skip
	v_mov_b32_e32 v2, s22
	s_waitcnt vmcnt(0)
	ds_write_b32 v2, v206
.Ltkt_a_skip:
	s_or_b64 exec, exec, s[0:1]
	v_mov_b32_e32 v2, s22
	s_waitcnt lgkmcnt(0)
	s_barrier
	ds_read_b32 v2, v2
	s_movk_i32 s0, 0x737
	s_waitcnt lgkmcnt(0)
	v_cmp_lt_i32_e32 vcc, s0, v2
	v_readfirstlane_b32 s29, v2
	s_mov_b64 s[0:1], -1
	s_cbranch_vccnz .LBB0_550
	v_mov_b32 v2, v0
	s_nop 0
	v_cmp_eq_u32_e32 vcc, 0, v2
	s_and_saveexec_b64 s[0:1], vcc
	s_cbranch_execz .LBB0_579
	s_mov_b64 s[30:31], exec
	v_mbcnt_lo_u32_b32 v2, s30, 0
	v_mbcnt_hi_u32_b32 v2, s31, v2
	v_cmp_eq_u32_e32 vcc, 0, v2
	s_and_saveexec_b64 s[14:15], vcc
	s_cbranch_execz .LBB0_557
	s_bcnt1_i32_b64 s9, s[30:31]
	v_mov_b32_e32 v3, s9
	global_atomic_add v206, v195, v3, s[48:49] offset:24 sc0
.LBB0_557:
	s_or_b64 exec, exec, s[14:15]
	s_or_b64 exec, exec, s[0:1]
	s_cmpk_gt_i32 s29, 0x20f
	s_mov_b64 s[0:1], -1
	s_cbranch_scc1 .LBB0_580
